# scan scores product (4 dependent MFMAs fed by just-in-time LDS reads) in S3 and S1 heavy items: all fragment reads issued up front using spare registers
# speedup vs baseline: 1.0111x; 1.0053x over previous
.LBB0_423:
	v_lshlrev_b32_e32 v10, 3, v13
	v_add_u32_e32 v8, s0, v10
	v_lshlrev_b32_e32 v9, 4, v8
	v_lshlrev_b32_e32 v11, 2, v216
	v_and_b32_e32 v9, 0xfffffc00, v9
	v_and_b32_e32 v11, 32, v11
	v_lshlrev_b32_e32 v15, 6, v216
	v_bitop3_b32 v8, v8, v11, 56 bitop3:0x6c
	v_add_u32_e32 v9, s1, v9
	v_add3_u32 v12, v9, v15, v8
	v_cvt_pk_bf16_f32 v8, v74, v75
	v_cvt_pk_bf16_f32 v9, v108, v109
	ds_write_b64 v12, v[8:9]
	v_cvt_pk_bf16_f32 v8, v106, v107
	v_cvt_pk_bf16_f32 v9, v104, v105
	ds_write_b64 v12, v[8:9] offset:4096
	v_cvt_pk_bf16_f32 v8, v102, v103
	v_cvt_pk_bf16_f32 v9, v98, v99
	ds_write_b64 v12, v[8:9] offset:8192
	v_cvt_pk_bf16_f32 v8, v96, v97
	v_cvt_pk_bf16_f32 v9, v94, v95
	ds_write_b64 v12, v[8:9] offset:12288
	v_cvt_pk_bf16_f32 v8, v92, v93
	v_cvt_pk_bf16_f32 v9, v90, v91
	ds_write_b64 v12, v[8:9] offset:16384
	v_cvt_pk_bf16_f32 v8, v88, v89
	v_cvt_pk_bf16_f32 v9, v86, v87
	ds_write_b64 v12, v[8:9] offset:20480
	v_cvt_pk_bf16_f32 v8, v84, v85
	v_cvt_pk_bf16_f32 v9, v82, v83
	ds_write_b64 v12, v[8:9] offset:24576
	v_cvt_pk_bf16_f32 v8, v78, v79
	v_cvt_pk_bf16_f32 v9, v76, v77
	ds_write_b64 v12, v[8:9] offset:28672
	s_waitcnt lgkmcnt(0)
	s_barrier
	v_xad_u32 v12, v217, v11, v15
	v_add_u32_e32 v8, s65, v12
	v_mov_b32_e32 v14, 0
	s_andn2_b64 vcc, exec, s[14:15]
	v_add_u32_e32 v9, s2, v12
	v_mov_b32_e32 v16, 0
	v_mov_b32_e32 v17, 0
	v_mov_b32_e32 v18, 0
	v_mov_b32_e32 v19, 0
	s_cbranch_vccnz .LBB0_425
	v_add_u32_e32 v28, s42, v8
	ds_read_b128 v[16:19], v28 offset:16384
	ds_read_b128 v[20:23], v9
	ds_read_b128 v[24:27], v28 offset:17408
	ds_read_b128 v[244:247], v9 offset:1024
	ds_read_b128 v[248:251], v28 offset:18432
	ds_read_b128 v[252:255], v9 offset:2048
	ds_read_b128 v[196:199], v28 offset:19456
	s_waitcnt lgkmcnt(5)
	v_mfma_f32_16x16x32_bf16 v[16:19], v[16:19], v[20:23], 0
	ds_read_b128 v[20:23], v9 offset:3072
	s_waitcnt lgkmcnt(4)
	v_mfma_f32_16x16x32_bf16 v[16:19], v[24:27], v[244:247], v[16:19]
	s_waitcnt lgkmcnt(2)
	v_mfma_f32_16x16x32_bf16 v[16:19], v[248:251], v[252:255], v[16:19]
	s_waitcnt lgkmcnt(0)
	v_mfma_f32_16x16x32_bf16 v[16:19], v[196:199], v[20:23], v[16:19]
	v_add_u32_e32 v20, s43, v110
	v_sub_u32_e32 v21, v111, v20
	v_cvt_f32_i32_e32 v21, v21
	v_cmp_ge_i32_e32 vcc, v111, v20
	v_or_b32_e32 v22, 3, v20
	v_or_b32_e32 v23, 2, v20
	v_mul_f32_e64 v21, -v174, v21
	v_mul_f32_e32 v21, 0x3fb8aa3b, v21
	v_exp_f32_e32 v21, v21
	s_nop 0
	v_mul_f32_e32 v16, v21, v16
	v_xad_u32 v21, v20, -1, v111
	v_cvt_f32_i32_e32 v21, v21
	v_cndmask_b32_e32 v16, 0, v16, vcc
	v_cmp_gt_i32_e32 vcc, v111, v20
	v_sub_u32_e32 v20, v111, v23
	v_mul_f32_e64 v21, -v174, v21
	v_mul_f32_e32 v21, 0x3fb8aa3b, v21
	v_exp_f32_e32 v21, v21
	v_cvt_f32_i32_e32 v20, v20
	v_mul_f32_e32 v17, v21, v17
	v_sub_u32_e32 v21, v111, v22
	v_cvt_f32_i32_e32 v21, v21
	v_mul_f32_e64 v20, -v174, v20
	v_mul_f32_e32 v20, 0x3fb8aa3b, v20
	v_exp_f32_e32 v20, v20
	v_mul_f32_e64 v21, -v174, v21
	v_mul_f32_e32 v21, 0x3fb8aa3b, v21
	v_exp_f32_e32 v21, v21
	v_cndmask_b32_e32 v17, 0, v17, vcc
	v_cmp_ge_i32_e32 vcc, v111, v23
	v_pk_mul_f32 v[18:19], v[20:21], v[18:19]
	s_nop 0
	v_cndmask_b32_e32 v18, 0, v18, vcc
	v_cmp_ge_i32_e32 vcc, v111, v22
	s_nop 1
	v_cndmask_b32_e32 v19, 0, v19, vcc
.LBB0_425:
	v_lshl_add_u32 v13, v13, 7, s44
	v_add_u32_e32 v15, s3, v15
	v_cvt_pk_bf16_f32 v16, v16, v17
	v_cvt_pk_bf16_f32 v17, v18, v19
	v_and_b32_e32 v13, 0xfffffc00, v13
	v_bitop3_b32 v18, v10, v11, 56 bitop3:0x6c
	v_add3_u32 v13, v15, v13, v18
	ds_write_b64 v13, v[16:17]
	s_andn2_b64 vcc, exec, s[16:17]
	v_mov_b32_e32 v13, 0
	v_mov_b32_e32 v16, 0
	v_mov_b32_e32 v17, 0
	s_cbranch_vccnz .LBB0_427
	v_add_u32_e32 v13, s45, v8
	ds_read_b128 v[16:19], v13 offset:16384
	ds_read_b128 v[20:23], v9
	ds_read_b128 v[24:27], v13 offset:17408
	ds_read_b128 v[244:247], v9 offset:1024
	ds_read_b128 v[248:251], v13 offset:18432
	ds_read_b128 v[252:255], v9 offset:2048
	ds_read_b128 v[196:199], v13 offset:19456
	s_waitcnt lgkmcnt(5)
	v_mfma_f32_16x16x32_bf16 v[16:19], v[16:19], v[20:23], 0
	ds_read_b128 v[20:23], v9 offset:3072
	s_waitcnt lgkmcnt(4)
	v_mfma_f32_16x16x32_bf16 v[16:19], v[24:27], v[244:247], v[16:19]
	s_waitcnt lgkmcnt(2)
	v_mfma_f32_16x16x32_bf16 v[16:19], v[248:251], v[252:255], v[16:19]
	s_waitcnt lgkmcnt(0)
	v_mfma_f32_16x16x32_bf16 v[16:19], v[196:199], v[20:23], v[16:19]
	v_add_u32_e32 v20, s46, v110
	v_sub_u32_e32 v13, v111, v20
	v_cvt_f32_i32_e32 v13, v13
	v_cmp_ge_i32_e32 vcc, v111, v20
	v_or_b32_e32 v21, 3, v20
	v_mul_f32_e64 v13, -v174, v13
	v_mul_f32_e32 v13, 0x3fb8aa3b, v13
	v_exp_f32_e32 v13, v13
	s_nop 0
	v_mul_f32_e32 v13, v13, v16
	v_cndmask_b32_e32 v14, 0, v13, vcc
	v_xad_u32 v13, v20, -1, v111
	v_cvt_f32_i32_e32 v13, v13
	v_cmp_gt_i32_e32 vcc, v111, v20
	v_or_b32_e32 v20, 2, v20
	v_sub_u32_e32 v16, v111, v20
	v_mul_f32_e64 v13, -v174, v13
	v_mul_f32_e32 v13, 0x3fb8aa3b, v13
	v_exp_f32_e32 v13, v13
	v_cvt_f32_i32_e32 v16, v16
	v_mul_f32_e32 v13, v13, v17
	v_sub_u32_e32 v17, v111, v21
	v_cvt_f32_i32_e32 v17, v17
	v_mul_f32_e64 v16, -v174, v16
	v_mul_f32_e32 v16, 0x3fb8aa3b, v16
	v_exp_f32_e32 v16, v16
	v_mul_f32_e64 v17, -v174, v17
	v_mul_f32_e32 v17, 0x3fb8aa3b, v17
	v_exp_f32_e32 v17, v17
	v_cndmask_b32_e32 v13, 0, v13, vcc
	v_cmp_ge_i32_e32 vcc, v111, v20
	v_pk_mul_f32 v[16:17], v[16:17], v[18:19]
	s_nop 0
	v_cndmask_b32_e32 v16, 0, v16, vcc
	v_cmp_ge_i32_e32 vcc, v111, v21
	s_nop 1
	v_cndmask_b32_e32 v17, 0, v17, vcc

.LBB0_451:
	v_add_u32_e32 v12, s26, v13
	s_waitcnt lgkmcnt(0)
	s_barrier
	v_add_u32_e32 v8, s25, v12
	ds_read_b128 v[16:19], v8
	v_lshlrev_b32_e32 v8, 3, v10
	v_add_u32_e32 v15, s22, v8
	v_lshlrev_b32_e32 v9, 4, v15
	v_and_b32_e32 v20, 0xfffffc00, v9
	v_lshlrev_b32_e32 v9, 2, v14
	v_and_b32_e32 v9, 32, v9
	v_lshlrev_b32_e32 v11, 6, v14
	v_bitop3_b32 v14, v15, v9, 56 bitop3:0x6c
	v_add_u32_e32 v15, s27, v20
	s_waitcnt lgkmcnt(0)
	v_pk_mul_f32 v[20:21], v[92:93], v[16:17]
	v_add3_u32 v22, v15, v11, v14
	v_pk_mul_f32 v[14:15], v[112:113], v[18:19]
	v_cvt_pk_bf16_f32 v20, v20, v21
	s_andn2_b64 vcc, exec, s[46:47]
	v_cvt_pk_bf16_f32 v21, v14, v15
	ds_write_b64 v22, v[20:21]
	v_pk_mul_f32 v[20:21], v[110:111], v[16:17]
	v_pk_mul_f32 v[14:15], v[108:109], v[18:19]
	v_cvt_pk_bf16_f32 v20, v20, v21
	s_nop 0
	v_cvt_pk_bf16_f32 v21, v14, v15
	ds_write_b64 v22, v[20:21] offset:4096
	v_pk_mul_f32 v[20:21], v[106:107], v[16:17]
	v_pk_mul_f32 v[14:15], v[104:105], v[18:19]
	v_cvt_pk_bf16_f32 v20, v20, v21
	s_nop 0
	v_cvt_pk_bf16_f32 v21, v14, v15
	ds_write_b64 v22, v[20:21] offset:8192
	v_pk_mul_f32 v[20:21], v[102:103], v[16:17]
	v_pk_mul_f32 v[14:15], v[100:101], v[18:19]
	v_cvt_pk_bf16_f32 v20, v20, v21
	s_nop 0
	v_cvt_pk_bf16_f32 v21, v14, v15
	ds_write_b64 v22, v[20:21] offset:12288
	v_pk_mul_f32 v[20:21], v[98:99], v[16:17]
	v_pk_mul_f32 v[14:15], v[96:97], v[18:19]
	v_cvt_pk_bf16_f32 v20, v20, v21
	s_nop 0
	v_cvt_pk_bf16_f32 v21, v14, v15
	ds_write_b64 v22, v[20:21] offset:16384
	v_pk_mul_f32 v[20:21], v[94:95], v[16:17]
	v_pk_mul_f32 v[14:15], v[90:91], v[18:19]
	v_cvt_pk_bf16_f32 v20, v20, v21
	s_nop 0
	v_cvt_pk_bf16_f32 v21, v14, v15
	ds_write_b64 v22, v[20:21] offset:20480
	v_pk_mul_f32 v[14:15], v[86:87], v[18:19]
	v_pk_mul_f32 v[20:21], v[88:89], v[16:17]
	v_pk_mul_f32 v[16:17], v[82:83], v[16:17]
	v_cvt_pk_bf16_f32 v20, v20, v21
	v_cvt_pk_bf16_f32 v21, v14, v15
	ds_write_b64 v22, v[20:21] offset:24576
	v_pk_mul_f32 v[14:15], v[80:81], v[18:19]
	v_cvt_pk_bf16_f32 v16, v16, v17
	v_xad_u32 v18, v13, v9, v11
	v_cvt_pk_bf16_f32 v17, v14, v15
	ds_write_b64 v22, v[16:17] offset:28672
	v_add_u32_e32 v16, s65, v18
	v_mov_b32_e32 v13, 0
	v_add_u32_e32 v17, s28, v18
	v_mov_b32_e32 v14, 0
	v_mov_b32_e32 v15, 0
	v_mov_b32_e32 v19, 0
	v_mov_b32_e32 v20, 0
	s_cbranch_vccnz .LBB0_453
	v_add_u32_e32 v14, s83, v16
	ds_read_b128 v[20:23], v14 offset:16384
	ds_read_b128 v[24:27], v17
	ds_read_b128 v[28:31], v14 offset:17408
	ds_read_b128 v[244:247], v17 offset:1024
	ds_read_b128 v[248:251], v14 offset:18432
	ds_read_b128 v[252:255], v17 offset:2048
	ds_read_b128 v[196:199], v14 offset:19456
	s_waitcnt lgkmcnt(5)
	v_mfma_f32_16x16x32_bf16 v[20:23], v[20:23], v[24:27], 0
	ds_read_b128 v[24:27], v17 offset:3072
	s_waitcnt lgkmcnt(4)
	v_mfma_f32_16x16x32_bf16 v[20:23], v[28:31], v[244:247], v[20:23]
	s_waitcnt lgkmcnt(2)
	v_mfma_f32_16x16x32_bf16 v[20:23], v[248:251], v[252:255], v[20:23]
	s_waitcnt lgkmcnt(0)
	v_mfma_f32_16x16x32_bf16 v[20:23], v[196:199], v[24:27], v[20:23]
	v_add_u32_e32 v24, s86, v116
	v_cmp_le_i32_e32 vcc, v24, v117
	v_or_b32_e32 v19, 2, v24
	s_nop 4
	v_cndmask_b32_e32 v14, 0, v20, vcc
	v_cmp_lt_i32_e32 vcc, v24, v117
	v_or_b32_e32 v20, 3, v24
	s_nop 0
	v_cndmask_b32_e32 v15, 0, v21, vcc
	v_cmp_le_i32_e32 vcc, v19, v117
	s_nop 1
	v_cndmask_b32_e32 v19, 0, v22, vcc
	v_cmp_le_i32_e32 vcc, v20, v117
	s_nop 1
	v_cndmask_b32_e32 v20, 0, v23, vcc
.LBB0_453:
	v_lshl_add_u32 v10, v10, 7, s87
	v_add_u32_e32 v11, s29, v11
	v_cvt_pk_bf16_f32 v14, v14, v15
	v_cvt_pk_bf16_f32 v15, v19, v20
	v_and_b32_e32 v10, 0xfffffc00, v10
	v_bitop3_b32 v19, v8, v9, 56 bitop3:0x6c
	v_add3_u32 v10, v11, v10, v19
	ds_write_b64 v10, v[14:15]
	s_andn2_b64 vcc, exec, s[48:49]
	v_mov_b32_e32 v10, 0
	v_mov_b32_e32 v14, 0
	v_mov_b32_e32 v15, 0
	s_cbranch_vccnz .LBB0_455
	v_add_u32_e32 v10, s90, v16
	ds_read_b128 v[20:23], v10 offset:16384
	ds_read_b128 v[24:27], v17
	ds_read_b128 v[28:31], v10 offset:17408
	ds_read_b128 v[244:247], v17 offset:1024
	ds_read_b128 v[248:251], v10 offset:18432
	ds_read_b128 v[252:255], v17 offset:2048
	ds_read_b128 v[196:199], v10 offset:19456
	v_add_u32_e32 v15, s91, v116
	v_cmp_le_i32_e32 vcc, v15, v117
	v_or_b32_e32 v14, 2, v15
	s_waitcnt lgkmcnt(5)
	v_mfma_f32_16x16x32_bf16 v[20:23], v[20:23], v[24:27], 0
	ds_read_b128 v[24:27], v17 offset:3072
	s_waitcnt lgkmcnt(4)
	v_mfma_f32_16x16x32_bf16 v[20:23], v[28:31], v[244:247], v[20:23]
	s_waitcnt lgkmcnt(2)
	v_mfma_f32_16x16x32_bf16 v[20:23], v[248:251], v[252:255], v[20:23]
	s_waitcnt lgkmcnt(0)
	v_mfma_f32_16x16x32_bf16 v[20:23], v[196:199], v[24:27], v[20:23]
	s_nop 7
	v_cndmask_b32_e32 v13, 0, v20, vcc
	v_cmp_lt_i32_e32 vcc, v15, v117
	v_or_b32_e32 v15, 3, v15
	s_nop 0
	v_cndmask_b32_e32 v10, 0, v21, vcc
	v_cmp_le_i32_e32 vcc, v14, v117
	s_nop 1
	v_cndmask_b32_e32 v14, 0, v22, vcc
	v_cmp_le_i32_e32 vcc, v15, v117
	s_nop 1
	v_cndmask_b32_e32 v15, 0, v23, vcc

.LBB0_513:
	v_lshlrev_b32_e32 v10, 3, v13
	v_add_u32_e32 v8, s64, v10
	v_lshlrev_b32_e32 v9, 4, v8
	v_lshlrev_b32_e32 v11, 2, v215
	v_and_b32_e32 v9, 0xfffffc00, v9
	v_and_b32_e32 v11, 32, v11
	v_lshlrev_b32_e32 v15, 6, v215
	v_bitop3_b32 v8, v8, v11, 56 bitop3:0x6c
	v_add_u32_e32 v9, s90, v9
	v_add3_u32 v12, v9, v15, v8
	v_cvt_pk_bf16_f32 v8, v86, v87
	v_cvt_pk_bf16_f32 v9, v120, v121
	ds_write_b64 v12, v[8:9]
	v_cvt_pk_bf16_f32 v8, v118, v119
	v_cvt_pk_bf16_f32 v9, v116, v117
	ds_write_b64 v12, v[8:9] offset:4096
	v_cvt_pk_bf16_f32 v8, v114, v115
	v_cvt_pk_bf16_f32 v9, v112, v113
	ds_write_b64 v12, v[8:9] offset:8192
	v_cvt_pk_bf16_f32 v8, v108, v109
	v_cvt_pk_bf16_f32 v9, v106, v107
	ds_write_b64 v12, v[8:9] offset:12288
	v_cvt_pk_bf16_f32 v8, v104, v105
	v_cvt_pk_bf16_f32 v9, v102, v103
	ds_write_b64 v12, v[8:9] offset:16384
	v_cvt_pk_bf16_f32 v8, v100, v101
	v_cvt_pk_bf16_f32 v9, v98, v99
	ds_write_b64 v12, v[8:9] offset:20480
	v_cvt_pk_bf16_f32 v8, v96, v97
	v_cvt_pk_bf16_f32 v9, v94, v95
	ds_write_b64 v12, v[8:9] offset:24576
	v_cvt_pk_bf16_f32 v8, v90, v91
	v_cvt_pk_bf16_f32 v9, v88, v89
	ds_write_b64 v12, v[8:9] offset:28672
	s_waitcnt lgkmcnt(0)
	s_barrier
	v_xad_u32 v12, v216, v11, v15
	v_add_u32_e32 v8, s65, v12
	v_mov_b32_e32 v14, 0
	s_andn2_b64 vcc, exec, s[42:43]
	v_add_u32_e32 v9, s91, v12
	v_mov_b32_e32 v16, 0
	v_mov_b32_e32 v17, 0
	v_mov_b32_e32 v18, 0
	v_mov_b32_e32 v19, 0
	s_cbranch_vccnz .LBB0_515
	v_add_u32_e32 v28, s26, v8
	ds_read_b128 v[16:19], v28 offset:16384
	ds_read_b128 v[20:23], v9
	ds_read_b128 v[24:27], v28 offset:17408
	ds_read_b128 v[244:247], v9 offset:1024
	ds_read_b128 v[248:251], v28 offset:18432
	ds_read_b128 v[252:255], v9 offset:2048
	ds_read_b128 v[196:199], v28 offset:19456
	s_waitcnt lgkmcnt(5)
	v_mfma_f32_16x16x32_bf16 v[16:19], v[16:19], v[20:23], 0
	ds_read_b128 v[20:23], v9 offset:3072
	s_waitcnt lgkmcnt(4)
	v_mfma_f32_16x16x32_bf16 v[16:19], v[24:27], v[244:247], v[16:19]
	s_waitcnt lgkmcnt(2)
	v_mfma_f32_16x16x32_bf16 v[16:19], v[248:251], v[252:255], v[16:19]
	s_waitcnt lgkmcnt(0)
	v_mfma_f32_16x16x32_bf16 v[16:19], v[196:199], v[20:23], v[16:19]
	v_add_u32_e32 v20, s27, v126
	v_sub_u32_e32 v21, v127, v20
	v_cvt_f32_i32_e32 v21, v21
	v_cmp_ge_i32_e32 vcc, v127, v20
	v_or_b32_e32 v22, 3, v20
	v_or_b32_e32 v23, 2, v20
	v_mul_f32_e64 v21, -v152, v21
	v_mul_f32_e32 v21, 0x3fb8aa3b, v21
	v_exp_f32_e32 v21, v21
	s_nop 0
	v_mul_f32_e32 v16, v21, v16
	v_xad_u32 v21, v20, -1, v127
	v_cvt_f32_i32_e32 v21, v21
	v_cndmask_b32_e32 v16, 0, v16, vcc
	v_cmp_gt_i32_e32 vcc, v127, v20
	v_sub_u32_e32 v20, v127, v23
	v_mul_f32_e64 v21, -v152, v21
	v_mul_f32_e32 v21, 0x3fb8aa3b, v21
	v_exp_f32_e32 v21, v21
	v_cvt_f32_i32_e32 v20, v20
	v_mul_f32_e32 v17, v21, v17
	v_sub_u32_e32 v21, v127, v22
	v_cvt_f32_i32_e32 v21, v21
	v_mul_f32_e64 v20, -v152, v20
	v_mul_f32_e32 v20, 0x3fb8aa3b, v20
	v_exp_f32_e32 v20, v20
	v_mul_f32_e64 v21, -v152, v21
	v_mul_f32_e32 v21, 0x3fb8aa3b, v21
	v_exp_f32_e32 v21, v21
	v_cndmask_b32_e32 v17, 0, v17, vcc
	v_cmp_ge_i32_e32 vcc, v127, v23
	v_pk_mul_f32 v[18:19], v[20:21], v[18:19]
	s_nop 0
	v_cndmask_b32_e32 v18, 0, v18, vcc
	v_cmp_ge_i32_e32 vcc, v127, v22
	s_nop 1
	v_cndmask_b32_e32 v19, 0, v19, vcc
.LBB0_515:
	v_lshl_add_u32 v13, v13, 7, s68
	v_add_u32_e32 v15, s92, v15
	v_cvt_pk_bf16_f32 v16, v16, v17
	v_cvt_pk_bf16_f32 v17, v18, v19
	v_and_b32_e32 v13, 0xfffffc00, v13
	v_bitop3_b32 v18, v10, v11, 56 bitop3:0x6c
	v_add3_u32 v13, v15, v13, v18
	ds_write_b64 v13, v[16:17]
	s_andn2_b64 vcc, exec, s[44:45]
	v_mov_b32_e32 v13, 0
	v_mov_b32_e32 v16, 0
	v_mov_b32_e32 v17, 0
	s_cbranch_vccnz .LBB0_517
	v_add_u32_e32 v13, s70, v8
	ds_read_b128 v[16:19], v13 offset:16384
	ds_read_b128 v[20:23], v9
	ds_read_b128 v[24:27], v13 offset:17408
	ds_read_b128 v[244:247], v9 offset:1024
	ds_read_b128 v[248:251], v13 offset:18432
	ds_read_b128 v[252:255], v9 offset:2048
	ds_read_b128 v[196:199], v13 offset:19456
	s_waitcnt lgkmcnt(5)
	v_mfma_f32_16x16x32_bf16 v[16:19], v[16:19], v[20:23], 0
	ds_read_b128 v[20:23], v9 offset:3072
	s_waitcnt lgkmcnt(4)
	v_mfma_f32_16x16x32_bf16 v[16:19], v[24:27], v[244:247], v[16:19]
	s_waitcnt lgkmcnt(2)
	v_mfma_f32_16x16x32_bf16 v[16:19], v[248:251], v[252:255], v[16:19]
	s_waitcnt lgkmcnt(0)
	v_mfma_f32_16x16x32_bf16 v[16:19], v[196:199], v[20:23], v[16:19]
	v_add_u32_e32 v20, s71, v126
	v_sub_u32_e32 v13, v127, v20
	v_cvt_f32_i32_e32 v13, v13
	v_cmp_ge_i32_e32 vcc, v127, v20
	v_or_b32_e32 v21, 3, v20
	v_mul_f32_e64 v13, -v152, v13
	v_mul_f32_e32 v13, 0x3fb8aa3b, v13
	v_exp_f32_e32 v13, v13
	s_nop 0
	v_mul_f32_e32 v13, v13, v16
	v_cndmask_b32_e32 v14, 0, v13, vcc
	v_xad_u32 v13, v20, -1, v127
	v_cvt_f32_i32_e32 v13, v13
	v_cmp_gt_i32_e32 vcc, v127, v20
	v_or_b32_e32 v20, 2, v20
	v_sub_u32_e32 v16, v127, v20
	v_mul_f32_e64 v13, -v152, v13
	v_mul_f32_e32 v13, 0x3fb8aa3b, v13
	v_exp_f32_e32 v13, v13
	v_cvt_f32_i32_e32 v16, v16
	v_mul_f32_e32 v13, v13, v17
	v_sub_u32_e32 v17, v127, v21
	v_cvt_f32_i32_e32 v17, v17
	v_mul_f32_e64 v16, -v152, v16
	v_mul_f32_e32 v16, 0x3fb8aa3b, v16
	v_exp_f32_e32 v16, v16
	v_mul_f32_e64 v17, -v152, v17
	v_mul_f32_e32 v17, 0x3fb8aa3b, v17
	v_exp_f32_e32 v17, v17
	v_cndmask_b32_e32 v13, 0, v13, vcc
	v_cmp_ge_i32_e32 vcc, v127, v20
	v_pk_mul_f32 v[16:17], v[16:17], v[18:19]
	s_nop 0
	v_cndmask_b32_e32 v16, 0, v16, vcc
	v_cmp_ge_i32_e32 vcc, v127, v21
	s_nop 1
	v_cndmask_b32_e32 v17, 0, v17, vcc

.LBB0_539:
	v_add_u32_e32 v12, s66, v13
	s_waitcnt lgkmcnt(0)
	s_barrier
	v_add_u32_e32 v8, s24, v12
	ds_read_b128 v[16:19], v8
	v_lshlrev_b32_e32 v8, 3, v10
	v_add_u32_e32 v15, s64, v8
	v_lshlrev_b32_e32 v9, 4, v15
	v_and_b32_e32 v20, 0xfffffc00, v9
	v_lshlrev_b32_e32 v9, 2, v14
	v_and_b32_e32 v9, 32, v9
	v_lshlrev_b32_e32 v11, 6, v14
	v_bitop3_b32 v14, v15, v9, 56 bitop3:0x6c
	v_add_u32_e32 v15, s90, v20
	s_waitcnt lgkmcnt(0)
	v_pk_mul_f32 v[20:21], v[106:107], v[16:17]
	v_add3_u32 v22, v15, v11, v14
	v_pk_mul_f32 v[14:15], v[130:131], v[18:19]
	v_cvt_pk_bf16_f32 v20, v20, v21
	s_andn2_b64 vcc, exec, s[42:43]
	v_cvt_pk_bf16_f32 v21, v14, v15
	ds_write_b64 v22, v[20:21]
	v_pk_mul_f32 v[20:21], v[128:129], v[16:17]
	v_pk_mul_f32 v[14:15], v[126:127], v[18:19]
	v_cvt_pk_bf16_f32 v20, v20, v21
	s_nop 0
	v_cvt_pk_bf16_f32 v21, v14, v15
	ds_write_b64 v22, v[20:21] offset:4096
	v_pk_mul_f32 v[20:21], v[120:121], v[16:17]
	v_pk_mul_f32 v[14:15], v[118:119], v[18:19]
	v_cvt_pk_bf16_f32 v20, v20, v21
	s_nop 0
	v_cvt_pk_bf16_f32 v21, v14, v15
	ds_write_b64 v22, v[20:21] offset:8192
	v_pk_mul_f32 v[20:21], v[116:117], v[16:17]
	v_pk_mul_f32 v[14:15], v[114:115], v[18:19]
	v_cvt_pk_bf16_f32 v20, v20, v21
	s_nop 0
	v_cvt_pk_bf16_f32 v21, v14, v15
	ds_write_b64 v22, v[20:21] offset:12288
	v_pk_mul_f32 v[20:21], v[112:113], v[16:17]
	v_pk_mul_f32 v[14:15], v[110:111], v[18:19]
	v_cvt_pk_bf16_f32 v20, v20, v21
	s_nop 0
	v_cvt_pk_bf16_f32 v21, v14, v15
	ds_write_b64 v22, v[20:21] offset:16384
	v_pk_mul_f32 v[20:21], v[108:109], v[16:17]
	v_pk_mul_f32 v[14:15], v[104:105], v[18:19]
	v_cvt_pk_bf16_f32 v20, v20, v21
	s_nop 0
	v_cvt_pk_bf16_f32 v21, v14, v15
	ds_write_b64 v22, v[20:21] offset:20480
	v_pk_mul_f32 v[14:15], v[100:101], v[18:19]
	v_pk_mul_f32 v[20:21], v[102:103], v[16:17]
	v_pk_mul_f32 v[16:17], v[96:97], v[16:17]
	v_cvt_pk_bf16_f32 v20, v20, v21
	v_cvt_pk_bf16_f32 v21, v14, v15
	ds_write_b64 v22, v[20:21] offset:24576
	v_pk_mul_f32 v[14:15], v[94:95], v[18:19]
	v_cvt_pk_bf16_f32 v16, v16, v17
	v_xad_u32 v18, v13, v9, v11
	v_cvt_pk_bf16_f32 v17, v14, v15
	ds_write_b64 v22, v[16:17] offset:28672
	v_add_u32_e32 v16, s65, v18
	v_mov_b32_e32 v13, 0
	v_add_u32_e32 v17, s91, v18
	v_mov_b32_e32 v14, 0
	v_mov_b32_e32 v15, 0
	v_mov_b32_e32 v19, 0
	v_mov_b32_e32 v20, 0
	s_cbranch_vccnz .LBB0_541
	v_add_u32_e32 v14, s26, v16
	ds_read_b128 v[20:23], v14 offset:16384
	ds_read_b128 v[24:27], v17
	ds_read_b128 v[28:31], v14 offset:17408
	ds_read_b128 v[244:247], v17 offset:1024
	ds_read_b128 v[248:251], v14 offset:18432
	ds_read_b128 v[252:255], v17 offset:2048
	ds_read_b128 v[196:199], v14 offset:19456
	s_waitcnt lgkmcnt(5)
	v_mfma_f32_16x16x32_bf16 v[20:23], v[20:23], v[24:27], 0
	ds_read_b128 v[24:27], v17 offset:3072
	s_waitcnt lgkmcnt(4)
	v_mfma_f32_16x16x32_bf16 v[20:23], v[28:31], v[244:247], v[20:23]
	s_waitcnt lgkmcnt(2)
	v_mfma_f32_16x16x32_bf16 v[20:23], v[248:251], v[252:255], v[20:23]
	s_waitcnt lgkmcnt(0)
	v_mfma_f32_16x16x32_bf16 v[20:23], v[196:199], v[24:27], v[20:23]
	v_add_u32_e32 v24, s27, v134
	v_cmp_le_i32_e32 vcc, v24, v135
	v_or_b32_e32 v19, 2, v24
	s_nop 4
	v_cndmask_b32_e32 v14, 0, v20, vcc
	v_cmp_lt_i32_e32 vcc, v24, v135
	v_or_b32_e32 v20, 3, v24
	s_nop 0
	v_cndmask_b32_e32 v15, 0, v21, vcc
	v_cmp_le_i32_e32 vcc, v19, v135
	s_nop 1
	v_cndmask_b32_e32 v19, 0, v22, vcc
	v_cmp_le_i32_e32 vcc, v20, v135
	s_nop 1
	v_cndmask_b32_e32 v20, 0, v23, vcc
.LBB0_541:
	v_lshl_add_u32 v10, v10, 7, s68
	v_add_u32_e32 v11, s92, v11
	v_cvt_pk_bf16_f32 v14, v14, v15
	v_cvt_pk_bf16_f32 v15, v19, v20
	v_and_b32_e32 v10, 0xfffffc00, v10
	v_bitop3_b32 v19, v8, v9, 56 bitop3:0x6c
	v_add3_u32 v10, v11, v10, v19
	ds_write_b64 v10, v[14:15]
	s_andn2_b64 vcc, exec, s[44:45]
	v_mov_b32_e32 v10, 0
	v_mov_b32_e32 v14, 0
	v_mov_b32_e32 v15, 0
	s_cbranch_vccnz .LBB0_543
	v_add_u32_e32 v10, s70, v16
	ds_read_b128 v[20:23], v10 offset:16384
	ds_read_b128 v[24:27], v17
	ds_read_b128 v[28:31], v10 offset:17408
	ds_read_b128 v[244:247], v17 offset:1024
	ds_read_b128 v[248:251], v10 offset:18432
	ds_read_b128 v[252:255], v17 offset:2048
	ds_read_b128 v[196:199], v10 offset:19456
	v_add_u32_e32 v15, s71, v134
	v_cmp_le_i32_e32 vcc, v15, v135
	v_or_b32_e32 v14, 2, v15
	s_waitcnt lgkmcnt(5)
	v_mfma_f32_16x16x32_bf16 v[20:23], v[20:23], v[24:27], 0
	ds_read_b128 v[24:27], v17 offset:3072
	s_waitcnt lgkmcnt(4)
	v_mfma_f32_16x16x32_bf16 v[20:23], v[28:31], v[244:247], v[20:23]
	s_waitcnt lgkmcnt(2)
	v_mfma_f32_16x16x32_bf16 v[20:23], v[248:251], v[252:255], v[20:23]
	s_waitcnt lgkmcnt(0)
	v_mfma_f32_16x16x32_bf16 v[20:23], v[196:199], v[24:27], v[20:23]
	s_nop 7
	v_cndmask_b32_e32 v13, 0, v20, vcc
	v_cmp_lt_i32_e32 vcc, v15, v135
	v_or_b32_e32 v15, 3, v15
	s_nop 0
	v_cndmask_b32_e32 v10, 0, v21, vcc
	v_cmp_le_i32_e32 vcc, v14, v135
	s_nop 1
	v_cndmask_b32_e32 v14, 0, v22, vcc
	v_cmp_le_i32_e32 vcc, v15, v135
	s_nop 1
	v_cndmask_b32_e32 v15, 0, v23, vcc

.LBB0_710:
	v_lshlrev_b32_e32 v10, 3, v13
	v_add_u32_e32 v8, s69, v10
	v_lshlrev_b32_e32 v9, 4, v8
	v_lshlrev_b32_e32 v11, 2, v192
	v_and_b32_e32 v9, 0xfffffc00, v9
	v_and_b32_e32 v11, 32, v11
	v_lshlrev_b32_e32 v15, 6, v192
	v_bitop3_b32 v8, v8, v11, 56 bitop3:0x6c
	v_add_u32_e32 v9, s64, v9
	v_add3_u32 v12, v9, v15, v8
	v_cvt_pk_bf16_f32 v8, v86, v87
	v_cvt_pk_bf16_f32 v9, v88, v89
	ds_write_b64 v12, v[8:9]
	v_cvt_pk_bf16_f32 v8, v90, v91
	v_cvt_pk_bf16_f32 v9, v92, v93
	ds_write_b64 v12, v[8:9] offset:4096
	v_cvt_pk_bf16_f32 v8, v94, v95
	v_cvt_pk_bf16_f32 v9, v96, v97
	ds_write_b64 v12, v[8:9] offset:8192
	v_cvt_pk_bf16_f32 v8, v98, v99
	v_cvt_pk_bf16_f32 v9, v100, v101
	ds_write_b64 v12, v[8:9] offset:12288
	v_cvt_pk_bf16_f32 v8, v102, v103
	v_cvt_pk_bf16_f32 v9, v104, v105
	ds_write_b64 v12, v[8:9] offset:16384
	v_cvt_pk_bf16_f32 v8, v106, v107
	v_cvt_pk_bf16_f32 v9, v108, v109
	ds_write_b64 v12, v[8:9] offset:20480
	v_cvt_pk_bf16_f32 v8, v110, v111
	v_cvt_pk_bf16_f32 v9, v112, v113
	ds_write_b64 v12, v[8:9] offset:24576
	v_cvt_pk_bf16_f32 v8, v114, v115
	v_cvt_pk_bf16_f32 v9, v116, v117
	ds_write_b64 v12, v[8:9] offset:28672
	s_waitcnt lgkmcnt(0)
	s_barrier
	v_xad_u32 v12, v193, v11, v15
	v_add_u32_e32 v8, s60, v12
	v_mov_b32_e32 v14, 0
	s_andn2_b64 vcc, exec, s[30:31]
	v_add_u32_e32 v9, s2, v12
	v_mov_b32_e32 v16, 0
	v_mov_b32_e32 v17, 0
	v_mov_b32_e32 v18, 0
	v_mov_b32_e32 v19, 0
	s_cbranch_vccnz .LBB0_712
	v_add_u32_e32 v28, s86, v8
	ds_read_b128 v[16:19], v28 offset:16384
	ds_read_b128 v[20:23], v9
	ds_read_b128 v[24:27], v28 offset:17408
	ds_read_b128 v[244:247], v9 offset:1024
	ds_read_b128 v[248:251], v28 offset:18432
	ds_read_b128 v[252:255], v9 offset:2048
	ds_read_b128 v[196:199], v28 offset:19456
	s_waitcnt lgkmcnt(5)
	v_mfma_f32_16x16x32_bf16 v[16:19], v[16:19], v[20:23], 0
	ds_read_b128 v[20:23], v9 offset:3072
	s_waitcnt lgkmcnt(4)
	v_mfma_f32_16x16x32_bf16 v[16:19], v[24:27], v[244:247], v[16:19]
	s_waitcnt lgkmcnt(2)
	v_mfma_f32_16x16x32_bf16 v[16:19], v[248:251], v[252:255], v[16:19]
	s_waitcnt lgkmcnt(0)
	v_mfma_f32_16x16x32_bf16 v[16:19], v[196:199], v[20:23], v[16:19]
	v_add_u32_e32 v20, s87, v120
	v_sub_u32_e32 v21, v121, v20
	v_cvt_f32_i32_e32 v21, v21
	v_cmp_ge_i32_e32 vcc, v121, v20
	v_or_b32_e32 v22, 3, v20
	v_or_b32_e32 v23, 2, v20
	v_mul_f32_e64 v21, -v64, v21
	v_mul_f32_e32 v21, 0x3fb8aa3b, v21
	v_exp_f32_e32 v21, v21
	s_nop 0
	v_mul_f32_e32 v16, v21, v16
	v_xad_u32 v21, v20, -1, v121
	v_cvt_f32_i32_e32 v21, v21
	v_cndmask_b32_e32 v16, 0, v16, vcc
	v_cmp_gt_i32_e32 vcc, v121, v20
	v_sub_u32_e32 v20, v121, v23
	v_mul_f32_e64 v21, -v64, v21
	v_mul_f32_e32 v21, 0x3fb8aa3b, v21
	v_exp_f32_e32 v21, v21
	v_cvt_f32_i32_e32 v20, v20
	v_mul_f32_e32 v17, v21, v17
	v_sub_u32_e32 v21, v121, v22
	v_cvt_f32_i32_e32 v21, v21
	v_mul_f32_e64 v20, -v64, v20
	v_mul_f32_e32 v20, 0x3fb8aa3b, v20
	v_exp_f32_e32 v20, v20
	v_mul_f32_e64 v21, -v64, v21
	v_mul_f32_e32 v21, 0x3fb8aa3b, v21
	v_exp_f32_e32 v21, v21
	v_cndmask_b32_e32 v17, 0, v17, vcc
	v_cmp_ge_i32_e32 vcc, v121, v23
	v_pk_mul_f32 v[18:19], v[20:21], v[18:19]
	s_nop 0
	v_cndmask_b32_e32 v18, 0, v18, vcc
	v_cmp_ge_i32_e32 vcc, v121, v22
	s_nop 1
	v_cndmask_b32_e32 v19, 0, v19, vcc
.LBB0_712:
	v_lshl_add_u32 v13, v13, 7, s63
	v_add_u32_e32 v15, s3, v15
	v_cvt_pk_bf16_f32 v16, v16, v17
	v_cvt_pk_bf16_f32 v17, v18, v19
	v_and_b32_e32 v13, 0xfffffc00, v13
	v_bitop3_b32 v18, v10, v11, 56 bitop3:0x6c
	v_add3_u32 v13, v15, v13, v18
	ds_write_b64 v13, v[16:17]
	s_andn2_b64 vcc, exec, s[34:35]
	v_mov_b32_e32 v13, 0
	v_mov_b32_e32 v16, 0
	v_mov_b32_e32 v17, 0
	s_cbranch_vccnz .LBB0_714
	v_add_u32_e32 v13, s65, v8
	ds_read_b128 v[16:19], v13 offset:16384
	ds_read_b128 v[20:23], v9
	ds_read_b128 v[24:27], v13 offset:17408
	ds_read_b128 v[244:247], v9 offset:1024
	ds_read_b128 v[248:251], v13 offset:18432
	ds_read_b128 v[252:255], v9 offset:2048
	ds_read_b128 v[196:199], v13 offset:19456
	s_waitcnt lgkmcnt(5)
	v_mfma_f32_16x16x32_bf16 v[16:19], v[16:19], v[20:23], 0
	ds_read_b128 v[20:23], v9 offset:3072
	s_waitcnt lgkmcnt(4)
	v_mfma_f32_16x16x32_bf16 v[16:19], v[24:27], v[244:247], v[16:19]
	s_waitcnt lgkmcnt(2)
	v_mfma_f32_16x16x32_bf16 v[16:19], v[248:251], v[252:255], v[16:19]
	s_waitcnt lgkmcnt(0)
	v_mfma_f32_16x16x32_bf16 v[16:19], v[196:199], v[20:23], v[16:19]
	v_add_u32_e32 v20, s90, v120
	v_sub_u32_e32 v13, v121, v20
	v_cvt_f32_i32_e32 v13, v13
	v_cmp_ge_i32_e32 vcc, v121, v20
	v_or_b32_e32 v21, 3, v20
	v_mul_f32_e64 v13, -v64, v13
	v_mul_f32_e32 v13, 0x3fb8aa3b, v13
	v_exp_f32_e32 v13, v13
	s_nop 0
	v_mul_f32_e32 v13, v13, v16
	v_cndmask_b32_e32 v14, 0, v13, vcc
	v_xad_u32 v13, v20, -1, v121
	v_cvt_f32_i32_e32 v13, v13
	v_cmp_gt_i32_e32 vcc, v121, v20
	v_or_b32_e32 v20, 2, v20
	v_sub_u32_e32 v16, v121, v20
	v_mul_f32_e64 v13, -v64, v13
	v_mul_f32_e32 v13, 0x3fb8aa3b, v13
	v_exp_f32_e32 v13, v13
	v_cvt_f32_i32_e32 v16, v16
	v_mul_f32_e32 v13, v13, v17
	v_sub_u32_e32 v17, v121, v21
	v_cvt_f32_i32_e32 v17, v17
	v_mul_f32_e64 v16, -v64, v16
	v_mul_f32_e32 v16, 0x3fb8aa3b, v16
	v_exp_f32_e32 v16, v16
	v_mul_f32_e64 v17, -v64, v17
	v_mul_f32_e32 v17, 0x3fb8aa3b, v17
	v_exp_f32_e32 v17, v17
	v_cndmask_b32_e32 v13, 0, v13, vcc
	v_cmp_ge_i32_e32 vcc, v121, v20
	v_pk_mul_f32 v[16:17], v[16:17], v[18:19]
	s_nop 0
	v_cndmask_b32_e32 v16, 0, v16, vcc
	v_cmp_ge_i32_e32 vcc, v121, v21
	s_nop 1
	v_cndmask_b32_e32 v17, 0, v17, vcc

.LBB0_738:
	v_add_u32_e32 v12, s70, v13
	s_waitcnt lgkmcnt(0)
	s_barrier
	v_add_u32_e32 v8, s67, v12
	ds_read_b128 v[16:19], v8
	v_lshlrev_b32_e32 v8, 3, v10
	v_add_u32_e32 v15, s69, v8
	v_lshlrev_b32_e32 v9, 4, v15
	v_and_b32_e32 v20, 0xfffffc00, v9
	v_lshlrev_b32_e32 v9, 2, v14
	v_and_b32_e32 v9, 32, v9
	v_lshlrev_b32_e32 v11, 6, v14
	v_bitop3_b32 v14, v15, v9, 56 bitop3:0x6c
	v_add_u32_e32 v15, s64, v20
	s_waitcnt lgkmcnt(0)
	v_pk_mul_f32 v[20:21], v[92:93], v[16:17]
	v_add3_u32 v22, v15, v11, v14
	v_pk_mul_f32 v[14:15], v[94:95], v[18:19]
	v_cvt_pk_bf16_f32 v20, v20, v21
	s_andn2_b64 vcc, exec, s[30:31]
	v_cvt_pk_bf16_f32 v21, v14, v15
	ds_write_b64 v22, v[20:21]
	v_pk_mul_f32 v[20:21], v[96:97], v[16:17]
	v_pk_mul_f32 v[14:15], v[98:99], v[18:19]
	v_cvt_pk_bf16_f32 v20, v20, v21
	s_nop 0
	v_cvt_pk_bf16_f32 v21, v14, v15
	ds_write_b64 v22, v[20:21] offset:4096
	v_pk_mul_f32 v[20:21], v[100:101], v[16:17]
	v_pk_mul_f32 v[14:15], v[102:103], v[18:19]
	v_cvt_pk_bf16_f32 v20, v20, v21
	s_nop 0
	v_cvt_pk_bf16_f32 v21, v14, v15
	ds_write_b64 v22, v[20:21] offset:8192
	v_pk_mul_f32 v[20:21], v[104:105], v[16:17]
	v_pk_mul_f32 v[14:15], v[106:107], v[18:19]
	v_cvt_pk_bf16_f32 v20, v20, v21
	s_nop 0
	v_cvt_pk_bf16_f32 v21, v14, v15
	ds_write_b64 v22, v[20:21] offset:12288
	v_pk_mul_f32 v[20:21], v[108:109], v[16:17]
	v_pk_mul_f32 v[14:15], v[110:111], v[18:19]
	v_cvt_pk_bf16_f32 v20, v20, v21
	s_nop 0
	v_cvt_pk_bf16_f32 v21, v14, v15
	ds_write_b64 v22, v[20:21] offset:16384
	v_pk_mul_f32 v[20:21], v[112:113], v[16:17]
	v_pk_mul_f32 v[14:15], v[114:115], v[18:19]
	v_cvt_pk_bf16_f32 v20, v20, v21
	s_nop 0
	v_cvt_pk_bf16_f32 v21, v14, v15
	ds_write_b64 v22, v[20:21] offset:20480
	v_pk_mul_f32 v[14:15], v[118:119], v[18:19]
	v_pk_mul_f32 v[20:21], v[116:117], v[16:17]
	v_pk_mul_f32 v[16:17], v[120:121], v[16:17]
	v_cvt_pk_bf16_f32 v20, v20, v21
	v_cvt_pk_bf16_f32 v21, v14, v15
	ds_write_b64 v22, v[20:21] offset:24576
	v_pk_mul_f32 v[14:15], v[122:123], v[18:19]
	v_cvt_pk_bf16_f32 v16, v16, v17
	v_xad_u32 v18, v13, v9, v11
	v_cvt_pk_bf16_f32 v17, v14, v15
	ds_write_b64 v22, v[16:17] offset:28672
	v_add_u32_e32 v16, s60, v18
	v_mov_b32_e32 v13, 0
	v_add_u32_e32 v17, s2, v18
	v_mov_b32_e32 v14, 0
	v_mov_b32_e32 v15, 0
	v_mov_b32_e32 v19, 0
	v_mov_b32_e32 v20, 0
	s_cbranch_vccnz .LBB0_740
	v_add_u32_e32 v14, s86, v16
	ds_read_b128 v[20:23], v14 offset:16384
	ds_read_b128 v[24:27], v17
	ds_read_b128 v[28:31], v14 offset:17408
	ds_read_b128 v[244:247], v17 offset:1024
	ds_read_b128 v[248:251], v14 offset:18432
	ds_read_b128 v[252:255], v17 offset:2048
	ds_read_b128 v[196:199], v14 offset:19456
	s_waitcnt lgkmcnt(5)
	v_mfma_f32_16x16x32_bf16 v[20:23], v[20:23], v[24:27], 0
	ds_read_b128 v[24:27], v17 offset:3072
	s_waitcnt lgkmcnt(4)
	v_mfma_f32_16x16x32_bf16 v[20:23], v[28:31], v[244:247], v[20:23]
	s_waitcnt lgkmcnt(2)
	v_mfma_f32_16x16x32_bf16 v[20:23], v[248:251], v[252:255], v[20:23]
	s_waitcnt lgkmcnt(0)
	v_mfma_f32_16x16x32_bf16 v[20:23], v[196:199], v[24:27], v[20:23]
	v_add_u32_e32 v24, s87, v124
	v_cmp_le_i32_e32 vcc, v24, v64
	v_or_b32_e32 v19, 2, v24
	s_nop 4
	v_cndmask_b32_e32 v14, 0, v20, vcc
	v_cmp_lt_i32_e32 vcc, v24, v64
	v_or_b32_e32 v20, 3, v24
	s_nop 0
	v_cndmask_b32_e32 v15, 0, v21, vcc
	v_cmp_le_i32_e32 vcc, v19, v64
	s_nop 1
	v_cndmask_b32_e32 v19, 0, v22, vcc
	v_cmp_le_i32_e32 vcc, v20, v64
	s_nop 1
	v_cndmask_b32_e32 v20, 0, v23, vcc
.LBB0_740:
	v_lshl_add_u32 v10, v10, 7, s63
	v_add_u32_e32 v11, s3, v11
	v_cvt_pk_bf16_f32 v14, v14, v15
	v_cvt_pk_bf16_f32 v15, v19, v20
	v_and_b32_e32 v10, 0xfffffc00, v10
	v_bitop3_b32 v19, v8, v9, 56 bitop3:0x6c
	v_add3_u32 v10, v11, v10, v19
	ds_write_b64 v10, v[14:15]
	s_andn2_b64 vcc, exec, s[34:35]
	v_mov_b32_e32 v10, 0
	v_mov_b32_e32 v14, 0
	v_mov_b32_e32 v15, 0
	s_cbranch_vccnz .LBB0_742
	v_add_u32_e32 v10, s65, v16
	ds_read_b128 v[20:23], v10 offset:16384
	ds_read_b128 v[24:27], v17
	ds_read_b128 v[28:31], v10 offset:17408
	ds_read_b128 v[244:247], v17 offset:1024
	ds_read_b128 v[248:251], v10 offset:18432
	ds_read_b128 v[252:255], v17 offset:2048
	ds_read_b128 v[196:199], v10 offset:19456
	v_add_u32_e32 v15, s90, v124
	v_cmp_le_i32_e32 vcc, v15, v64
	v_or_b32_e32 v14, 2, v15
	s_waitcnt lgkmcnt(5)
	v_mfma_f32_16x16x32_bf16 v[20:23], v[20:23], v[24:27], 0
	ds_read_b128 v[24:27], v17 offset:3072
	s_waitcnt lgkmcnt(4)
	v_mfma_f32_16x16x32_bf16 v[20:23], v[28:31], v[244:247], v[20:23]
	s_waitcnt lgkmcnt(2)
	v_mfma_f32_16x16x32_bf16 v[20:23], v[248:251], v[252:255], v[20:23]
	s_waitcnt lgkmcnt(0)
	v_mfma_f32_16x16x32_bf16 v[20:23], v[196:199], v[24:27], v[20:23]
	s_nop 7
	v_cndmask_b32_e32 v13, 0, v20, vcc
	v_cmp_lt_i32_e32 vcc, v15, v64
	v_or_b32_e32 v15, 3, v15
	s_nop 0
	v_cndmask_b32_e32 v10, 0, v21, vcc
	v_cmp_le_i32_e32 vcc, v14, v64
	s_nop 1
	v_cndmask_b32_e32 v14, 0, v22, vcc
	v_cmp_le_i32_e32 vcc, v15, v64
	s_nop 1
	v_cndmask_b32_e32 v15, 0, v23, vcc
